# rope epilogue: 32 dwordx2 stores per lane merged into 16 dwordx4 via v_permlane16_swap pairs (o1/o2 halves exchanged between fq-adjacent lanes)
# speedup vs baseline: 1.0115x; 1.0086x over previous
; #define PG8_ST8(rs, b0, p, v) __builtin_amdgcn_raw_buffer_store_b64(v, rs, (int)((const char*)(p) - (const char*)(b0)), 0, 16)
; __device__ __forceinline__ unsigned cvt_pk_bf16(float lo, float hi) { unsigned r; asm volatile("v_cvt_pk_bf16_f32 %0, %1, %2" : "=v"(r) : "v"(lo), "v"(hi)); return r; }
;     __device__ __forceinline__ void operator()(const f32x4 (&acc)[2][2][4][2], const Unit& u, int wr, int wc, int fr, int fq) const {
;     ...
;                 for (int m = 0; m < 4; ++m) { const int row = row0 + ai * HALF + m * 16;
;                     const f32x4 cc = c4[m] * sc, ss = s4[m] * sc;
;                     bf16_t* rowp = P + (size_t)row * ldp + col0;
; #pragma unroll
;                     for (int bj = 0; bj < 2; ++bj) { const f32x4 x1 = acc[ai][bj][m][0], x2 = acc[ai][bj][m][1]; const f32x4 o1 = x1 * cc - x2 * ss, o2 = x2 * cc + x1 * ss;
;                         u32x2 w1, w2; w1.x = cvt_pk_bf16(o1[0], o1[1]); w1.y = cvt_pk_bf16(o1[2], o1[3]); w2.x = cvt_pk_bf16(o2[0], o2[1]); w2.y = cvt_pk_bf16(o2[2], o2[3]);
;                         PG8_ST8(rsp_, P, rowp + bj * HALF, w1); PG8_ST8(rsp_, P, rowp + bj * HALF + 32, w2); } }
.LBB0_230:
	v_lshl_add_u32 v164, s27, 8, v175
	s_add_i32 s27, s62, s56
	s_cmp_gt_i32 s27, 3
	s_mov_b64 s[34:35], -1
	s_cbranch_scc0 .LBB0_237
	s_cmp_lg_u32 s27, 8
	s_cselect_b64 s[34:35], -1, 0
	s_cmp_lt_u32 s27, 15
	s_cselect_b64 s[36:37], -1, 0
	s_and_b64 s[36:37], s[34:35], s[36:37]
	s_mov_b64 s[34:35], -1
	s_and_b64 vcc, exec, s[36:37]
	v_add_u32_e32 v172, 0x80, v164
	v_add_u32_e32 v170, 0x90, v164
	v_add_u32_e32 v168, 0xa0, v164
	v_add_u32_e32 v166, 0xb0, v164
	s_cbranch_vccz .LBB0_233
	s_cmp_lt_u32 s27, 7
	s_cselect_b64 s[34:35], -1, 0
	s_add_i32 s36, s27, -9
	s_cmp_lt_u32 s36, 3
	s_cselect_b64 s[36:37], -1, 0
	s_or_b64 vcc, s[34:35], s[36:37]
	v_mov_b32_e32 v132, 0x3e38aa3b
	v_ashrrev_i32_e32 v165, 31, v164
	v_cndmask_b32_e32 v174, 1.0, v132, vcc
	v_lshlrev_b64 v[132:133], 7, v[164:165]
	v_lshl_add_u64 v[134:135], v[154:155], 0, v[132:133]
	v_lshl_add_u64 v[132:133], v[156:157], 0, v[132:133]
	global_load_dwordx4 v[176:179], v[134:135], off
	global_load_dwordx4 v[184:187], v[132:133], off
	v_or_b32_e32 v192, 16, v164
	v_ashrrev_i32_e32 v193, 31, v192
	v_lshlrev_b64 v[132:133], 7, v[192:193]
	v_lshl_add_u64 v[134:135], v[154:155], 0, v[132:133]
	v_lshl_add_u64 v[132:133], v[156:157], 0, v[132:133]
	global_load_dwordx4 v[188:191], v[134:135], off
	global_load_dwordx4 v[218:221], v[132:133], off
	v_or_b32_e32 v182, 32, v164
	v_ashrrev_i32_e32 v183, 31, v182
	v_lshlrev_b64 v[132:133], 7, v[182:183]
	v_lshl_add_u64 v[134:135], v[154:155], 0, v[132:133]
	v_lshl_add_u64 v[132:133], v[156:157], 0, v[132:133]
	global_load_dwordx4 v[144:147], v[134:135], off
	global_load_dwordx4 v[140:143], v[132:133], off
	v_or_b32_e32 v180, 48, v164
	v_ashrrev_i32_e32 v181, 31, v180
	v_lshlrev_b64 v[132:133], 7, v[180:181]
	v_lshl_add_u64 v[134:135], v[154:155], 0, v[132:133]
	v_lshl_add_u64 v[132:133], v[156:157], 0, v[132:133]
	global_load_dwordx4 v[136:139], v[134:135], off
	s_movk_i32 s36, 0x2400
	global_load_dwordx4 v[132:135], v[132:133], off
	v_ashrrev_i32_e32 v173, 31, v172
	v_ashrrev_i32_e32 v171, 31, v170
	v_ashrrev_i32_e32 v169, 31, v168
	v_ashrrev_i32_e32 v167, 31, v166
	s_waitcnt vmcnt(0)
	v_pk_mul_f32 v[198:199], v[174:175], v[178:179] op_sel_hi:[0,1]
	v_pk_mul_f32 v[186:187], v[174:175], v[186:187] op_sel_hi:[0,1]
	v_pk_mul_f32 v[184:185], v[174:175], v[184:185] op_sel_hi:[0,1]
	v_pk_mul_f32 v[200:201], v[174:175], v[176:177] op_sel_hi:[0,1]
	v_mov_b64_e32 v[176:177], s[20:21]
	v_pk_mul_f32 v[208:209], v[118:119], v[186:187]
	v_pk_mul_f32 v[222:223], v[116:117], v[184:185]
	v_mad_i64_i32 v[204:205], s[34:35], v164, s36, v[176:177]
	v_lshl_or_b32 v178, s27, 9, v202
	v_mov_b32_e32 v179, v2
	v_bfe_u32 v244, v215, 4, 1
	v_mul_u32_u24_e32 v244, 56, v244
	v_add_u32_e32 v178, v178, v244
	v_pk_fma_f32 v[208:209], v[126:127], v[198:199], v[208:209] neg_lo:[0,0,1] neg_hi:[0,0,1]
	v_pk_fma_f32 v[222:223], v[124:125], v[200:201], v[222:223] neg_lo:[0,0,1] neg_hi:[0,0,1]
	v_pk_mul_f32 v[224:225], v[126:127], v[186:187]
	v_pk_mul_f32 v[226:227], v[124:125], v[184:185]
	v_lshl_add_u64 v[204:205], v[204:205], 0, v[178:179]
	v_pk_fma_f32 v[224:225], v[118:119], v[198:199], v[224:225]
	v_pk_fma_f32 v[226:227], v[116:117], v[200:201], v[226:227]
	v_cvt_pk_bf16_f32 v222, v222, v223
	v_cvt_pk_bf16_f32 v223, v208, v209
	v_mad_i64_i32 v[192:193], s[34:35], v192, s36, v[176:177]
	v_cvt_pk_bf16_f32 v208, v226, v227
	v_cvt_pk_bf16_f32 v209, v224, v225
	v_mov_b32_e32 v228, v222
	v_mov_b32_e32 v229, v223
	v_mov_b32_e32 v230, v208
	v_mov_b32_e32 v231, v209
	s_nop 1
	v_permlane16_swap_b32_e32 v228, v230
	v_permlane16_swap_b32_e32 v229, v231
	global_store_dwordx4 v[204:205], v[228:231], off
	v_pk_mul_f32 v[208:209], v[122:123], v[186:187]
	v_pk_mul_f32 v[222:223], v[120:121], v[184:185]
	v_pk_mul_f32 v[186:187], v[130:131], v[186:187]
	v_pk_mul_f32 v[184:185], v[128:129], v[184:185]
	v_pk_fma_f32 v[186:187], v[122:123], v[198:199], v[186:187]
	v_pk_fma_f32 v[184:185], v[120:121], v[200:201], v[184:185]
	v_pk_fma_f32 v[208:209], v[130:131], v[198:199], v[208:209] neg_lo:[0,0,1] neg_hi:[0,0,1]
	v_pk_fma_f32 v[222:223], v[128:129], v[200:201], v[222:223] neg_lo:[0,0,1] neg_hi:[0,0,1]
	v_lshl_add_u64 v[192:193], v[192:193], 0, v[178:179]
	v_cvt_pk_bf16_f32 v198, v222, v223
	v_cvt_pk_bf16_f32 v199, v208, v209
	v_cvt_pk_bf16_f32 v184, v184, v185
	v_cvt_pk_bf16_f32 v185, v186, v187
	v_pk_mul_f32 v[186:187], v[174:175], v[190:191] op_sel_hi:[0,1]
	v_pk_mul_f32 v[190:191], v[174:175], v[218:219] op_sel_hi:[0,1]
	v_mov_b32_e32 v232, v198
	v_mov_b32_e32 v233, v199
	v_mov_b32_e32 v234, v184
	v_mov_b32_e32 v235, v185
	s_nop 1
	v_permlane16_swap_b32_e32 v232, v234
	v_permlane16_swap_b32_e32 v233, v235
	global_store_dwordx4 v[204:205], v[232:235], off offset:256
	v_pk_mul_f32 v[184:185], v[174:175], v[188:189] op_sel_hi:[0,1]
	v_pk_mul_f32 v[188:189], v[174:175], v[220:221] op_sel_hi:[0,1]
	v_pk_mul_f32 v[198:199], v[100:101], v[190:191]
	v_pk_mul_f32 v[200:201], v[102:103], v[188:189]
	v_pk_fma_f32 v[198:199], v[108:109], v[184:185], v[198:199] neg_lo:[0,0,1] neg_hi:[0,0,1]
	v_pk_fma_f32 v[200:201], v[110:111], v[186:187], v[200:201] neg_lo:[0,0,1] neg_hi:[0,0,1]
	v_pk_mul_f32 v[204:205], v[108:109], v[190:191]
	v_pk_mul_f32 v[208:209], v[110:111], v[188:189]
	v_cvt_pk_bf16_f32 v198, v198, v199
	v_cvt_pk_bf16_f32 v199, v200, v201
	v_pk_fma_f32 v[204:205], v[100:101], v[184:185], v[204:205]
	v_pk_fma_f32 v[208:209], v[102:103], v[186:187], v[208:209]
	v_cvt_pk_bf16_f32 v200, v204, v205
	v_pk_mul_f32 v[142:143], v[174:175], v[142:143] op_sel_hi:[0,1]
	v_cvt_pk_bf16_f32 v201, v208, v209
	v_mov_b32_e32 v236, v198
	v_mov_b32_e32 v237, v199
	v_mov_b32_e32 v238, v200
	v_mov_b32_e32 v239, v201
; #define PG8_ST8(rs, b0, p, v) __builtin_amdgcn_raw_buffer_store_b64(v, rs, (int)((const char*)(p) - (const char*)(b0)), 0, 16)
; __device__ __forceinline__ unsigned cvt_pk_bf16(float lo, float hi) { unsigned r; asm volatile("v_cvt_pk_bf16_f32 %0, %1, %2" : "=v"(r) : "v"(lo), "v"(hi)); return r; }
;     __device__ __forceinline__ void operator()(const f32x4 (&acc)[2][2][4][2], const Unit& u, int wr, int wc, int fr, int fq) const {
;     ...
;                 for (int m = 0; m < 4; ++m) { const int row = row0 + ai * HALF + m * 16; c4[m] = *(const f32x4*)(rc + (size_t)row * 32 + f); s4[m] = *(const f32x4*)(rs + (size_t)row * 32 + f); }
;                 asm volatile("" ::: "memory");
; #pragma unroll
;                 for (int m = 0; m < 4; ++m) { const int row = row0 + ai * HALF + m * 16;
;                     const f32x4 cc = c4[m] * sc, ss = s4[m] * sc;
;                     bf16_t* rowp = P + (size_t)row * ldp + col0;
; #pragma unroll
;                     for (int bj = 0; bj < 2; ++bj) { const f32x4 x1 = acc[ai][bj][m][0], x2 = acc[ai][bj][m][1]; const f32x4 o1 = x1 * cc - x2 * ss, o2 = x2 * cc + x1 * ss;
;                         u32x2 w1, w2; w1.x = cvt_pk_bf16(o1[0], o1[1]); w1.y = cvt_pk_bf16(o1[2], o1[3]); w2.x = cvt_pk_bf16(o2[0], o2[1]); w2.y = cvt_pk_bf16(o2[2], o2[3]);
;                         PG8_ST8(rsp_, P, rowp + bj * HALF, w1); PG8_ST8(rsp_, P, rowp + bj * HALF + 32, w2); } }
	s_nop 1
	v_permlane16_swap_b32_e32 v236, v238
	v_permlane16_swap_b32_e32 v237, v239
	global_store_dwordx4 v[192:193], v[236:239], off
	v_pk_mul_f32 v[198:199], v[104:105], v[190:191]
	v_pk_mul_f32 v[190:191], v[112:113], v[190:191]
	v_pk_mul_f32 v[200:201], v[106:107], v[188:189]
	v_pk_fma_f32 v[198:199], v[112:113], v[184:185], v[198:199] neg_lo:[0,0,1] neg_hi:[0,0,1]
	v_pk_mul_f32 v[188:189], v[114:115], v[188:189]
	v_pk_fma_f32 v[184:185], v[104:105], v[184:185], v[190:191]
	v_pk_fma_f32 v[200:201], v[114:115], v[186:187], v[200:201] neg_lo:[0,0,1] neg_hi:[0,0,1]
	v_pk_fma_f32 v[186:187], v[106:107], v[186:187], v[188:189]
	v_cvt_pk_bf16_f32 v188, v198, v199
	v_cvt_pk_bf16_f32 v189, v200, v201
	v_cvt_pk_bf16_f32 v184, v184, v185
	v_pk_mul_f32 v[140:141], v[174:175], v[140:141] op_sel_hi:[0,1]
	v_cvt_pk_bf16_f32 v185, v186, v187
	v_mov_b32_e32 v240, v188
	v_mov_b32_e32 v241, v189
	v_mov_b32_e32 v242, v184
	v_mov_b32_e32 v243, v185
	s_nop 1
	v_permlane16_swap_b32_e32 v240, v242
	v_permlane16_swap_b32_e32 v241, v243
	global_store_dwordx4 v[192:193], v[240:243], off offset:256
	v_pk_mul_f32 v[144:145], v[174:175], v[144:145] op_sel_hi:[0,1]
	v_pk_mul_f32 v[146:147], v[174:175], v[146:147] op_sel_hi:[0,1]
	v_pk_mul_f32 v[184:185], v[84:85], v[140:141]
	v_pk_mul_f32 v[186:187], v[86:87], v[142:143]
	v_mad_i64_i32 v[182:183], s[34:35], v182, s36, v[176:177]
	v_pk_fma_f32 v[186:187], v[94:95], v[146:147], v[186:187] neg_lo:[0,0,1] neg_hi:[0,0,1]
	v_pk_fma_f32 v[184:185], v[92:93], v[144:145], v[184:185] neg_lo:[0,0,1] neg_hi:[0,0,1]
	v_pk_mul_f32 v[188:189], v[92:93], v[140:141]
	v_pk_mul_f32 v[190:191], v[94:95], v[142:143]
	v_lshl_add_u64 v[182:183], v[182:183], 0, v[178:179]
	v_pk_fma_f32 v[190:191], v[86:87], v[146:147], v[190:191]
	v_pk_fma_f32 v[188:189], v[84:85], v[144:145], v[188:189]
	v_cvt_pk_bf16_f32 v184, v184, v185
	v_cvt_pk_bf16_f32 v185, v186, v187
	v_pk_mul_f32 v[134:135], v[174:175], v[134:135] op_sel_hi:[0,1]
	v_cvt_pk_bf16_f32 v186, v188, v189
	v_cvt_pk_bf16_f32 v187, v190, v191
	v_mov_b32_e32 v228, v184
	v_mov_b32_e32 v229, v185
	v_mov_b32_e32 v230, v186
	v_mov_b32_e32 v231, v187
	s_nop 1
	v_permlane16_swap_b32_e32 v228, v230
	v_permlane16_swap_b32_e32 v229, v231
	global_store_dwordx4 v[182:183], v[228:231], off
	v_pk_mul_f32 v[184:185], v[88:89], v[140:141]
	v_pk_mul_f32 v[186:187], v[90:91], v[142:143]
	v_pk_mul_f32 v[140:141], v[96:97], v[140:141]
	v_pk_mul_f32 v[142:143], v[98:99], v[142:143]
	v_pk_fma_f32 v[186:187], v[98:99], v[146:147], v[186:187] neg_lo:[0,0,1] neg_hi:[0,0,1]
	v_pk_fma_f32 v[184:185], v[96:97], v[144:145], v[184:185] neg_lo:[0,0,1] neg_hi:[0,0,1]
	v_pk_fma_f32 v[142:143], v[90:91], v[146:147], v[142:143]
	v_pk_fma_f32 v[140:141], v[88:89], v[144:145], v[140:141]
	v_cvt_pk_bf16_f32 v144, v184, v185
	v_cvt_pk_bf16_f32 v145, v186, v187
	v_pk_mul_f32 v[132:133], v[174:175], v[132:133] op_sel_hi:[0,1]
	v_cvt_pk_bf16_f32 v140, v140, v141
	v_cvt_pk_bf16_f32 v141, v142, v143
	v_mov_b32_e32 v232, v144
	v_mov_b32_e32 v233, v145
	v_mov_b32_e32 v234, v140
	v_mov_b32_e32 v235, v141
	s_nop 1
	v_permlane16_swap_b32_e32 v232, v234
	v_permlane16_swap_b32_e32 v233, v235
	global_store_dwordx4 v[182:183], v[232:235], off offset:256
	v_pk_mul_f32 v[136:137], v[174:175], v[136:137] op_sel_hi:[0,1]
	v_pk_mul_f32 v[138:139], v[174:175], v[138:139] op_sel_hi:[0,1]
	v_pk_mul_f32 v[142:143], v[68:69], v[132:133]
	v_pk_mul_f32 v[144:145], v[70:71], v[134:135]
	v_mad_i64_i32 v[140:141], s[34:35], v180, s36, v[176:177]
	v_pk_fma_f32 v[144:145], v[78:79], v[138:139], v[144:145] neg_lo:[0,0,1] neg_hi:[0,0,1]
	v_pk_fma_f32 v[142:143], v[76:77], v[136:137], v[142:143] neg_lo:[0,0,1] neg_hi:[0,0,1]
	v_pk_mul_f32 v[146:147], v[76:77], v[132:133]
	v_pk_mul_f32 v[180:181], v[78:79], v[134:135]
	v_lshl_add_u64 v[140:141], v[140:141], 0, v[178:179]
	v_pk_fma_f32 v[180:181], v[70:71], v[138:139], v[180:181]
	v_pk_fma_f32 v[146:147], v[68:69], v[136:137], v[146:147]
	v_cvt_pk_bf16_f32 v142, v142, v143
	v_cvt_pk_bf16_f32 v143, v144, v145
	v_lshlrev_b64 v[184:185], 7, v[168:169]
	v_cvt_pk_bf16_f32 v144, v146, v147
	v_cvt_pk_bf16_f32 v145, v180, v181
	v_mov_b32_e32 v236, v142
	v_mov_b32_e32 v237, v143
	v_mov_b32_e32 v238, v144
	v_mov_b32_e32 v239, v145
	s_nop 1
	v_permlane16_swap_b32_e32 v236, v238
	v_permlane16_swap_b32_e32 v237, v239
	global_store_dwordx4 v[140:141], v[236:239], off
	v_pk_mul_f32 v[142:143], v[72:73], v[132:133]
	v_pk_mul_f32 v[144:145], v[74:75], v[134:135]
	v_pk_mul_f32 v[132:133], v[80:81], v[132:133]
	v_pk_fma_f32 v[144:145], v[82:83], v[138:139], v[144:145] neg_lo:[0,0,1] neg_hi:[0,0,1]
	v_pk_fma_f32 v[142:143], v[80:81], v[136:137], v[142:143] neg_lo:[0,0,1] neg_hi:[0,0,1]
	v_pk_mul_f32 v[134:135], v[82:83], v[134:135]
	v_pk_fma_f32 v[132:133], v[72:73], v[136:137], v[132:133]
	v_cvt_pk_bf16_f32 v136, v142, v143
	v_cvt_pk_bf16_f32 v137, v144, v145
	v_pk_fma_f32 v[134:135], v[74:75], v[138:139], v[134:135]
	v_cvt_pk_bf16_f32 v132, v132, v133
	v_lshlrev_b64 v[144:145], 7, v[170:171]
	v_cvt_pk_bf16_f32 v133, v134, v135
	v_mov_b32_e32 v240, v136
	v_mov_b32_e32 v241, v137
	v_mov_b32_e32 v242, v132
	v_mov_b32_e32 v243, v133
	s_nop 1
	v_permlane16_swap_b32_e32 v240, v242
	v_permlane16_swap_b32_e32 v241, v243
	global_store_dwordx4 v[140:141], v[240:243], off offset:256
	v_lshlrev_b64 v[136:137], 7, v[172:173]
	v_lshl_add_u64 v[132:133], v[154:155], 0, v[136:137]
	v_lshl_add_u64 v[136:137], v[156:157], 0, v[136:137]
	global_load_dwordx4 v[132:135], v[132:133], off
	v_lshl_add_u64 v[140:141], v[154:155], 0, v[144:145]
	global_load_dwordx4 v[136:139], v[136:137], off
	v_lshl_add_u64 v[144:145], v[156:157], 0, v[144:145]
	global_load_dwordx4 v[140:143], v[140:141], off
	v_lshl_add_u64 v[180:181], v[154:155], 0, v[184:185]
	global_load_dwordx4 v[144:147], v[144:145], off
	v_lshl_add_u64 v[184:185], v[156:157], 0, v[184:185]
	global_load_dwordx4 v[180:183], v[180:181], off
	v_lshlrev_b64 v[192:193], 7, v[166:167]
	global_load_dwordx4 v[184:187], v[184:185], off
	v_lshl_add_u64 v[188:189], v[154:155], 0, v[192:193]
	v_lshl_add_u64 v[192:193], v[156:157], 0, v[192:193]
	global_load_dwordx4 v[188:191], v[188:189], off
	global_load_dwordx4 v[218:221], v[192:193], off
	s_waitcnt vmcnt(0)
; #define PG8_ST8(rs, b0, p, v) __builtin_amdgcn_raw_buffer_store_b64(v, rs, (int)((const char*)(p) - (const char*)(b0)), 0, 16)
; __device__ __forceinline__ unsigned cvt_pk_bf16(float lo, float hi) { unsigned r; asm volatile("v_cvt_pk_bf16_f32 %0, %1, %2" : "=v"(r) : "v"(lo), "v"(hi)); return r; }
;     __device__ __forceinline__ void operator()(const f32x4 (&acc)[2][2][4][2], const Unit& u, int wr, int wc, int fr, int fq) const {
;     ...
;                 for (int m = 0; m < 4; ++m) { const int row = row0 + ai * HALF + m * 16;
;                     const f32x4 cc = c4[m] * sc, ss = s4[m] * sc;
;                     bf16_t* rowp = P + (size_t)row * ldp + col0;
; #pragma unroll
;                     for (int bj = 0; bj < 2; ++bj) { const f32x4 x1 = acc[ai][bj][m][0], x2 = acc[ai][bj][m][1]; const f32x4 o1 = x1 * cc - x2 * ss, o2 = x2 * cc + x1 * ss;
;                         u32x2 w1, w2; w1.x = cvt_pk_bf16(o1[0], o1[1]); w1.y = cvt_pk_bf16(o1[2], o1[3]); w2.x = cvt_pk_bf16(o2[0], o2[1]); w2.y = cvt_pk_bf16(o2[2], o2[3]);
;                         PG8_ST8(rsp_, P, rowp + bj * HALF, w1); PG8_ST8(rsp_, P, rowp + bj * HALF + 32, w2); } }
	v_pk_mul_f32 v[132:133], v[174:175], v[132:133] op_sel_hi:[0,1]
	v_pk_mul_f32 v[138:139], v[174:175], v[138:139] op_sel_hi:[0,1]
	v_pk_mul_f32 v[136:137], v[174:175], v[136:137] op_sel_hi:[0,1]
	v_pk_mul_f32 v[134:135], v[174:175], v[134:135] op_sel_hi:[0,1]
	v_pk_mul_f32 v[198:199], v[52:53], v[136:137]
	v_pk_mul_f32 v[200:201], v[54:55], v[138:139]
	v_mad_i64_i32 v[192:193], s[34:35], v172, s36, v[176:177]
	v_pk_fma_f32 v[200:201], v[62:63], v[134:135], v[200:201] neg_lo:[0,0,1] neg_hi:[0,0,1]
	v_pk_fma_f32 v[198:199], v[60:61], v[132:133], v[198:199] neg_lo:[0,0,1] neg_hi:[0,0,1]
	v_pk_mul_f32 v[204:205], v[60:61], v[136:137]
	v_pk_mul_f32 v[208:209], v[62:63], v[138:139]
	v_lshl_add_u64 v[192:193], v[192:193], 0, v[178:179]
	v_pk_fma_f32 v[208:209], v[54:55], v[134:135], v[208:209]
	v_pk_fma_f32 v[204:205], v[52:53], v[132:133], v[204:205]
	v_cvt_pk_bf16_f32 v198, v198, v199
	v_cvt_pk_bf16_f32 v199, v200, v201
	s_nop 0
	v_cvt_pk_bf16_f32 v200, v204, v205
	v_cvt_pk_bf16_f32 v201, v208, v209
	v_mov_b32_e32 v228, v198
	v_mov_b32_e32 v229, v199
	v_mov_b32_e32 v230, v200
	v_mov_b32_e32 v231, v201
	s_nop 1
	v_permlane16_swap_b32_e32 v228, v230
	v_permlane16_swap_b32_e32 v229, v231
	global_store_dwordx4 v[192:193], v[228:231], off
	v_pk_mul_f32 v[198:199], v[56:57], v[136:137]
	v_pk_mul_f32 v[200:201], v[58:59], v[138:139]
	v_pk_mul_f32 v[136:137], v[64:65], v[136:137]
	v_pk_fma_f32 v[200:201], v[66:67], v[134:135], v[200:201] neg_lo:[0,0,1] neg_hi:[0,0,1]
	v_pk_fma_f32 v[198:199], v[64:65], v[132:133], v[198:199] neg_lo:[0,0,1] neg_hi:[0,0,1]
	v_pk_mul_f32 v[138:139], v[66:67], v[138:139]
	v_pk_fma_f32 v[132:133], v[56:57], v[132:133], v[136:137]
	v_cvt_pk_bf16_f32 v136, v198, v199
	v_cvt_pk_bf16_f32 v137, v200, v201
	v_pk_fma_f32 v[134:135], v[58:59], v[134:135], v[138:139]
	v_cvt_pk_bf16_f32 v132, v132, v133
	v_pk_mul_f32 v[138:139], v[174:175], v[144:145] op_sel_hi:[0,1]
	v_cvt_pk_bf16_f32 v133, v134, v135
	v_mov_b32_e32 v232, v136
	v_mov_b32_e32 v233, v137
	v_mov_b32_e32 v234, v132
	v_mov_b32_e32 v235, v133
	s_nop 1
	v_permlane16_swap_b32_e32 v232, v234
	v_permlane16_swap_b32_e32 v233, v235
	global_store_dwordx4 v[192:193], v[232:235], off offset:256
	v_pk_mul_f32 v[136:137], v[174:175], v[146:147] op_sel_hi:[0,1]
	v_pk_mul_f32 v[132:133], v[174:175], v[140:141] op_sel_hi:[0,1]
	v_pk_mul_f32 v[134:135], v[174:175], v[142:143] op_sel_hi:[0,1]
	v_pk_mul_f32 v[142:143], v[36:37], v[138:139]
	v_pk_mul_f32 v[144:145], v[38:39], v[136:137]
	v_mad_i64_i32 v[140:141], s[34:35], v170, s36, v[176:177]
	v_pk_fma_f32 v[144:145], v[46:47], v[134:135], v[144:145] neg_lo:[0,0,1] neg_hi:[0,0,1]
	v_pk_fma_f32 v[142:143], v[44:45], v[132:133], v[142:143] neg_lo:[0,0,1] neg_hi:[0,0,1]
	v_pk_mul_f32 v[146:147], v[44:45], v[138:139]
	v_pk_mul_f32 v[192:193], v[46:47], v[136:137]
	v_lshl_add_u64 v[140:141], v[140:141], 0, v[178:179]
	v_pk_fma_f32 v[192:193], v[38:39], v[134:135], v[192:193]
	v_pk_fma_f32 v[146:147], v[36:37], v[132:133], v[146:147]
	v_cvt_pk_bf16_f32 v142, v142, v143
	v_cvt_pk_bf16_f32 v143, v144, v145
	s_nop 0
	v_cvt_pk_bf16_f32 v144, v146, v147
	v_cvt_pk_bf16_f32 v145, v192, v193
	v_mov_b32_e32 v236, v142
	v_mov_b32_e32 v237, v143
	v_mov_b32_e32 v238, v144
	v_mov_b32_e32 v239, v145
	s_nop 1
	v_permlane16_swap_b32_e32 v236, v238
	v_permlane16_swap_b32_e32 v237, v239
	global_store_dwordx4 v[140:141], v[236:239], off
	v_pk_mul_f32 v[142:143], v[40:41], v[138:139]
	v_pk_mul_f32 v[144:145], v[42:43], v[136:137]
	v_pk_mul_f32 v[138:139], v[48:49], v[138:139]
	v_pk_mul_f32 v[136:137], v[50:51], v[136:137]
	v_pk_fma_f32 v[144:145], v[50:51], v[134:135], v[144:145] neg_lo:[0,0,1] neg_hi:[0,0,1]
	v_pk_fma_f32 v[142:143], v[48:49], v[132:133], v[142:143] neg_lo:[0,0,1] neg_hi:[0,0,1]
	v_pk_fma_f32 v[134:135], v[42:43], v[134:135], v[136:137]
	v_pk_fma_f32 v[132:133], v[40:41], v[132:133], v[138:139]
	v_cvt_pk_bf16_f32 v136, v142, v143
	v_cvt_pk_bf16_f32 v137, v144, v145
	v_pk_mul_f32 v[138:139], v[174:175], v[184:185] op_sel_hi:[0,1]
	v_cvt_pk_bf16_f32 v132, v132, v133
	v_cvt_pk_bf16_f32 v133, v134, v135
	v_mov_b32_e32 v240, v136
	v_mov_b32_e32 v241, v137
	v_mov_b32_e32 v242, v132
	v_mov_b32_e32 v243, v133
	s_nop 1
	v_permlane16_swap_b32_e32 v240, v242
	v_permlane16_swap_b32_e32 v241, v243
; #define PG8_ST8(rs, b0, p, v) __builtin_amdgcn_raw_buffer_store_b64(v, rs, (int)((const char*)(p) - (const char*)(b0)), 0, 16)
; __device__ __forceinline__ unsigned cvt_pk_bf16(float lo, float hi) { unsigned r; asm volatile("v_cvt_pk_bf16_f32 %0, %1, %2" : "=v"(r) : "v"(lo), "v"(hi)); return r; }
;     __device__ __forceinline__ void operator()(const f32x4 (&acc)[2][2][4][2], const Unit& u, int wr, int wc, int fr, int fq) const {
;     ...
;                 for (int m = 0; m < 4; ++m) { const int row = row0 + ai * HALF + m * 16;
;                     const f32x4 cc = c4[m] * sc, ss = s4[m] * sc;
;                     bf16_t* rowp = P + (size_t)row * ldp + col0;
; #pragma unroll
;                     for (int bj = 0; bj < 2; ++bj) { const f32x4 x1 = acc[ai][bj][m][0], x2 = acc[ai][bj][m][1]; const f32x4 o1 = x1 * cc - x2 * ss, o2 = x2 * cc + x1 * ss;
;                         u32x2 w1, w2; w1.x = cvt_pk_bf16(o1[0], o1[1]); w1.y = cvt_pk_bf16(o1[2], o1[3]); w2.x = cvt_pk_bf16(o2[0], o2[1]); w2.y = cvt_pk_bf16(o2[2], o2[3]);
;                         PG8_ST8(rsp_, P, rowp + bj * HALF, w1); PG8_ST8(rsp_, P, rowp + bj * HALF + 32, w2); } }
	global_store_dwordx4 v[140:141], v[240:243], off offset:256
	v_pk_mul_f32 v[136:137], v[174:175], v[186:187] op_sel_hi:[0,1]
	v_pk_mul_f32 v[132:133], v[174:175], v[180:181] op_sel_hi:[0,1]
	v_pk_mul_f32 v[134:135], v[174:175], v[182:183] op_sel_hi:[0,1]
	v_pk_mul_f32 v[142:143], v[20:21], v[138:139]
	v_pk_mul_f32 v[144:145], v[22:23], v[136:137]
	v_mad_i64_i32 v[140:141], s[34:35], v168, s36, v[176:177]
	v_pk_fma_f32 v[144:145], v[30:31], v[134:135], v[144:145] neg_lo:[0,0,1] neg_hi:[0,0,1]
	v_pk_fma_f32 v[142:143], v[28:29], v[132:133], v[142:143] neg_lo:[0,0,1] neg_hi:[0,0,1]
	v_pk_mul_f32 v[146:147], v[28:29], v[138:139]
	v_pk_mul_f32 v[180:181], v[30:31], v[136:137]
	v_lshl_add_u64 v[140:141], v[140:141], 0, v[178:179]
	v_pk_fma_f32 v[180:181], v[22:23], v[134:135], v[180:181]
	v_pk_fma_f32 v[146:147], v[20:21], v[132:133], v[146:147]
	v_cvt_pk_bf16_f32 v142, v142, v143
	v_cvt_pk_bf16_f32 v143, v144, v145
	s_nop 0
	v_cvt_pk_bf16_f32 v144, v146, v147
	v_cvt_pk_bf16_f32 v145, v180, v181
	v_mov_b32_e32 v228, v142
	v_mov_b32_e32 v229, v143
	v_mov_b32_e32 v230, v144
	v_mov_b32_e32 v231, v145
	s_nop 1
	v_permlane16_swap_b32_e32 v228, v230
	v_permlane16_swap_b32_e32 v229, v231
	global_store_dwordx4 v[140:141], v[228:231], off
	v_pk_mul_f32 v[142:143], v[24:25], v[138:139]
	v_pk_mul_f32 v[144:145], v[26:27], v[136:137]
	v_pk_mul_f32 v[138:139], v[32:33], v[138:139]
	v_pk_mul_f32 v[136:137], v[34:35], v[136:137]
	v_pk_fma_f32 v[144:145], v[34:35], v[134:135], v[144:145] neg_lo:[0,0,1] neg_hi:[0,0,1]
	v_pk_fma_f32 v[142:143], v[32:33], v[132:133], v[142:143] neg_lo:[0,0,1] neg_hi:[0,0,1]
	v_pk_fma_f32 v[134:135], v[26:27], v[134:135], v[136:137]
	v_pk_fma_f32 v[132:133], v[24:25], v[132:133], v[138:139]
	v_cvt_pk_bf16_f32 v136, v142, v143
	v_cvt_pk_bf16_f32 v137, v144, v145
	v_pk_mul_f32 v[138:139], v[174:175], v[218:219] op_sel_hi:[0,1]
	v_cvt_pk_bf16_f32 v132, v132, v133
	v_cvt_pk_bf16_f32 v133, v134, v135
	v_mov_b32_e32 v232, v136
	v_mov_b32_e32 v233, v137
	v_mov_b32_e32 v234, v132
	v_mov_b32_e32 v235, v133
	s_nop 1
	v_permlane16_swap_b32_e32 v232, v234
	v_permlane16_swap_b32_e32 v233, v235
	global_store_dwordx4 v[140:141], v[232:235], off offset:256
	v_pk_mul_f32 v[136:137], v[174:175], v[220:221] op_sel_hi:[0,1]
	v_pk_mul_f32 v[132:133], v[174:175], v[188:189] op_sel_hi:[0,1]
	v_pk_mul_f32 v[134:135], v[174:175], v[190:191] op_sel_hi:[0,1]
	v_pk_mul_f32 v[142:143], v[4:5], v[138:139]
	v_pk_mul_f32 v[144:145], v[6:7], v[136:137]
	v_mad_i64_i32 v[140:141], s[34:35], v166, s36, v[176:177]
	v_pk_fma_f32 v[144:145], v[14:15], v[134:135], v[144:145] neg_lo:[0,0,1] neg_hi:[0,0,1]
	v_pk_fma_f32 v[142:143], v[12:13], v[132:133], v[142:143] neg_lo:[0,0,1] neg_hi:[0,0,1]
	v_pk_mul_f32 v[146:147], v[12:13], v[138:139]
	v_pk_mul_f32 v[176:177], v[14:15], v[136:137]
	v_lshl_add_u64 v[140:141], v[140:141], 0, v[178:179]
	v_pk_fma_f32 v[176:177], v[6:7], v[134:135], v[176:177]
	v_pk_fma_f32 v[146:147], v[4:5], v[132:133], v[146:147]
	v_cvt_pk_bf16_f32 v142, v142, v143
	v_cvt_pk_bf16_f32 v143, v144, v145
	s_mov_b64 s[34:35], 0
	v_cvt_pk_bf16_f32 v144, v146, v147
	v_cvt_pk_bf16_f32 v145, v176, v177
	v_mov_b32_e32 v236, v142
	v_mov_b32_e32 v237, v143
	v_mov_b32_e32 v238, v144
	v_mov_b32_e32 v239, v145
	s_nop 1
	v_permlane16_swap_b32_e32 v236, v238
	v_permlane16_swap_b32_e32 v237, v239
	global_store_dwordx4 v[140:141], v[236:239], off
	v_pk_mul_f32 v[142:143], v[8:9], v[138:139]
	v_pk_mul_f32 v[144:145], v[10:11], v[136:137]
	v_pk_mul_f32 v[138:139], v[16:17], v[138:139]
	v_pk_mul_f32 v[136:137], v[18:19], v[136:137]
	v_pk_fma_f32 v[144:145], v[18:19], v[134:135], v[144:145] neg_lo:[0,0,1] neg_hi:[0,0,1]
	v_pk_fma_f32 v[142:143], v[16:17], v[132:133], v[142:143] neg_lo:[0,0,1] neg_hi:[0,0,1]
	v_pk_fma_f32 v[134:135], v[10:11], v[134:135], v[136:137]
	v_pk_fma_f32 v[132:133], v[8:9], v[132:133], v[138:139]
	v_cvt_pk_bf16_f32 v136, v142, v143
	v_cvt_pk_bf16_f32 v137, v144, v145
	s_nop 0
	v_cvt_pk_bf16_f32 v132, v132, v133
	v_cvt_pk_bf16_f32 v133, v134, v135
	v_mov_b32_e32 v240, v136
	v_mov_b32_e32 v241, v137
	v_mov_b32_e32 v242, v132
	v_mov_b32_e32 v243, v133
	s_nop 1
	v_permlane16_swap_b32_e32 v240, v242
	v_permlane16_swap_b32_e32 v241, v243
	global_store_dwordx4 v[140:141], v[240:243], off offset:256
